# speedup vs baseline: 1.0317x; 1.0039x over previous
.Lmy_z0:
	v_readfirstlane_b32 s14, v0
	s_load_dwordx2 s[4:5], s[0:1], 0x0
	s_load_dwordx4 s[8:11], s[0:1], 0x18
	s_load_dwordx2 s[6:7], s[0:1], 0x40
	s_lshr_b32 s28, s14, 8
	s_lshl_b32 s20, s2, 1
	s_add_i32 s12, s28, s20
	s_lshr_b32 s2, s14, 1
	v_and_b32_e32 v174, 31, v0
	v_bfe_u32 v164, v0, 5, 1
	s_and_b32 s15, s2, 0x60
	s_ashr_i32 s13, s12, 31
	v_or_b32_e32 v1, s15, v174
	v_lshlrev_b32_e32 v2, 3, v164
	s_lshl_b64 s[2:3], s[12:13], 13
	v_lshl_or_b32 v3, v1, 4, v2
	v_lshl_or_b32 v118, v1, 6, s2
	v_mov_b32_e32 v119, s3
	s_waitcnt lgkmcnt(0)
	global_load_dwordx2 v[66:67], v3, s[6:7]
	v_lshl_add_u64 v[4:5], v[118:119], 1, s[4:5]
	v_mov_b32_e32 v3, 0
	v_lshlrev_b32_e32 v2, 4, v164
	v_lshl_add_u64 v[2:3], v[4:5], 0, v[2:3]
	global_load_dwordx4 v[110:113], v[2:3], off
	global_load_dwordx4 v[106:109], v[2:3], off offset:32
	global_load_dwordx4 v[102:105], v[2:3], off offset:64
	global_load_dwordx4 v[98:101], v[2:3], off offset:96
	s_load_dwordx2 s[4:5], s[0:1], 0x30
	s_movk_i32 s2, 0xff
	v_cmp_lt_u32_e32 vcc, s2, v0
	s_and_saveexec_b64 s[2:3], vcc
	s_xor_b64 s[6:7], exec, s[2:3]
	s_cbranch_execz .LBB2_14
	s_movk_i32 s2, 0x1ff
	v_cmp_lt_u32_e64 s[2:3], s2, v0
	s_and_saveexec_b64 s[16:17], s[2:3]
	s_xor_b64 s[16:17], exec, s[16:17]
	s_cbranch_execz .LBB2_11
	s_movk_i32 s2, 0x2ff
	v_cmp_lt_u32_e64 s[2:3], s2, v0
	s_and_saveexec_b64 s[18:19], s[2:3]
	s_xor_b64 s[18:19], exec, s[18:19]
	s_cbranch_execz .LBB2_8
	s_movk_i32 s2, 0x33f
	v_cmp_lt_u32_e64 s[2:3], s2, v0
	v_mov_b32_e32 v3, 0
	s_and_saveexec_b64 s[22:23], s[2:3]
	s_xor_b64 s[2:3], exec, s[22:23]
	s_cbranch_execz .LBB2_5
	v_lshlrev_b32_e32 v2, 2, v0
	s_movk_i32 s22, 0xf300
	s_waitcnt lgkmcnt(0)
	v_lshl_add_u64 v[2:3], s[4:5], 0, v[2:3]
	s_mov_b32 s23, -1
	v_lshl_add_u64 v[4:5], v[2:3], 0, s[22:23]

.LBB2_79:
	v_lshrrev_b32_e32 v2, 2, v0
	v_and_b32_e32 v3, 3, v0
	s_add_i32 s21, 0, 0x16000
	v_mul_u32_u24_e32 v2, 0x90, v2
	v_lshlrev_b32_e32 v160, 2, v3
	v_add3_u32 v2, s21, v2, v160
	v_add_u32_e32 v2, 0x80, v2
	s_waitcnt vmcnt(11)
	v_permlane32_swap_b32_e32 v110, v112
	v_permlane32_swap_b32_e32 v111, v113
	v_permlane32_swap_b32_e32 v106, v108
	v_permlane32_swap_b32_e32 v107, v109
	v_permlane32_swap_b32_e32 v102, v104
	v_permlane32_swap_b32_e32 v103, v105
	v_permlane32_swap_b32_e32 v98, v100
	v_permlane32_swap_b32_e32 v99, v101
	ds_write2st64_b32 v2, v8, v9 offset1:72
	v_lshl_add_u32 v125, v4, 1, 0
	s_waitcnt vmcnt(8)
	s_waitcnt lgkmcnt(0)
	s_barrier
	ds_read_b128 v[2:5], v125
	ds_read_b128 v[18:21], v125 offset:1024
	s_waitcnt lgkmcnt(1)
	v_mfma_f32_32x32x16_f16 v[2:17], v[2:5], v[110:113], 0
	v_mul_u32_u24_e32 v165, 0x48, v164
	v_lshl_add_u32 v173, v165, 1, s21
	s_mul_i32 s18, s28, 0x4800
	s_add_i32 s18, s21, s18
	s_movk_i32 s23, 0x90
	v_lshlrev_b32_e32 v69, 4, v164
	s_mul_i32 s20, s28, 0x4400
	s_waitcnt lgkmcnt(0)
	v_mfma_f32_32x32x16_f16 v[2:17], v[18:21], v[106:109], v[2:17]
	ds_read_b128 v[18:21], v125 offset:2048
	ds_read_b128 v[22:25], v125 offset:3072
	ds_read_b128 v[34:37], v125 offset:9216
	ds_read_b128 v[38:41], v125 offset:10240
	s_add_i32 s20, s20, 0
	s_add_i32 s20, s20, 0x1f000
	s_lshl_b32 s15, s15, 1
	s_add_i32 s15, s20, s15
	s_waitcnt lgkmcnt(3)
	v_mfma_f32_32x32x16_f16 v[2:17], v[18:21], v[102:105], v[2:17]
	ds_read_b128 v[18:21], v125 offset:8192
	ds_read_b128 v[72:75], v125 offset:4096
	ds_read_b128 v[76:79], v125 offset:5120
	v_add_u32_e32 v167, s15, v69
	s_movk_i32 s15, 0x110
	s_load_dwordx8 s[4:11], s[0:1], 0x88
	v_lshlrev_b32_e32 v126, 2, v164
	s_mov_b32 s19, 0
	s_waitcnt lgkmcnt(0)
	v_mfma_f32_32x32x16_f16 v[2:17], v[22:25], v[98:101], v[2:17]
	s_and_b64 vcc, exec, s[2:3]
	v_mfma_f32_32x32x16_f16 v[18:33], v[18:21], v[110:113], 0
	v_mfma_f32_32x32x16_f16 v[18:33], v[34:37], v[106:109], v[18:33]
	ds_read_b128 v[80:83], v173 offset:128
	ds_read_b128 v[34:37], v125 offset:11264
	ds_read_b128 v[84:87], v125 offset:6144
	ds_read_b128 v[88:91], v125 offset:7168
	ds_read_b128 v[92:95], v173 offset:416
	s_waitcnt lgkmcnt(4)
	s_nop 2
	v_fmamk_f32 v68, v80, 0x3eb8aa3b, v2
	v_fmamk_f32 v70, v81, 0x3eb8aa3b, v3
	v_fmamk_f32 v4, v82, 0x3eb8aa3b, v4
	v_mfma_f32_32x32x16_f16 v[18:33], v[38:41], v[102:105], v[18:33]
	ds_read_b128 v[114:117], v173 offset:704
	ds_read_b128 v[128:131], v173 offset:992
	ds_read_b128 v[38:41], v125 offset:12288
	ds_read_b128 v[62:65], v173 offset:1280
	ds_read_b128 v[58:61], v173 offset:1568
	ds_read_b128 v[54:57], v173 offset:1856
	ds_read_b128 v[50:53], v173 offset:2144
	ds_read_b128 v[132:135], v125 offset:13312
	ds_read_b128 v[136:139], v173 offset:2432
	ds_read_b128 v[140:143], v125 offset:14336
	ds_read_b128 v[144:147], v125 offset:15360
	ds_read_b128 v[148:151], v173 offset:2720
	v_fmamk_f32 v5, v83, 0x3eb8aa3b, v5
	s_waitcnt lgkmcnt(12)
	v_fmamk_f32 v6, v92, 0x3eb8aa3b, v6
	v_fmamk_f32 v7, v93, 0x3eb8aa3b, v7
	v_fmamk_f32 v8, v94, 0x3eb8aa3b, v8
	v_mfma_f32_32x32x16_f16 v[18:33], v[34:37], v[98:101], v[18:33]
	v_fmamk_f32 v9, v95, 0x3eb8aa3b, v9
	s_waitcnt lgkmcnt(11)
	v_fmamk_f32 v10, v114, 0x3eb8aa3b, v10
	v_fmamk_f32 v11, v115, 0x3eb8aa3b, v11
	v_fmamk_f32 v12, v116, 0x3eb8aa3b, v12
	v_fmamk_f32 v13, v117, 0x3eb8aa3b, v13
	s_waitcnt lgkmcnt(10)
	v_fmamk_f32 v14, v128, 0x3eb8aa3b, v14
	v_fmamk_f32 v15, v129, 0x3eb8aa3b, v15
	s_waitcnt lgkmcnt(9)
	v_mfma_f32_32x32x16_f16 v[34:49], v[38:41], v[110:113], 0
	s_waitcnt lgkmcnt(3)
	v_add_f32_e32 v2, v18, v136
	v_add_f32_e32 v3, v19, v137
	v_add_f32_e32 v71, v20, v138
	v_add_f32_e32 v80, v21, v139
	ds_read_b128 v[18:21], v173 offset:3008
	s_waitcnt lgkmcnt(1)
	v_add_f32_e32 v81, v22, v148
	v_add_f32_e32 v96, v23, v149
	v_mfma_f32_32x32x16_f16 v[34:49], v[132:135], v[106:109], v[34:49]
	v_add_f32_e32 v97, v24, v150
	v_add_f32_e32 v122, v25, v151
	ds_read_b128 v[22:25], v173 offset:3296
	s_waitcnt lgkmcnt(1)
	v_add_f32_e32 v123, v26, v18
	v_add_f32_e32 v127, v27, v19
	v_add_f32_e32 v132, v28, v20
	v_add_f32_e32 v133, v29, v21
	v_mfma_f32_32x32x16_f16 v[34:49], v[140:143], v[102:105], v[34:49]
	s_waitcnt lgkmcnt(0)
	v_add_f32_e32 v134, v30, v22
	v_add_f32_e32 v135, v31, v23
	v_add_f32_e32 v136, v32, v24
	v_add_f32_e32 v137, v33, v25
	ds_read_b128 v[18:21], v173 offset:3584
	ds_read_b128 v[22:25], v173 offset:3872
	v_fmamk_f32 v16, v130, 0x3eb8aa3b, v16
	v_fmac_f32_e32 v17, 0x3eb8aa3b, v131
	v_mfma_f32_32x32x16_f16 v[34:49], v[144:147], v[98:101], v[34:49]
	s_waitcnt lgkmcnt(1)
	s_nop 10
	v_add_f32_e32 v138, v34, v18
	v_add_f32_e32 v139, v35, v19
	v_add_f32_e32 v140, v36, v20
	v_add_f32_e32 v141, v37, v21
	s_waitcnt lgkmcnt(0)
	v_add_f32_e32 v38, v38, v22
	ds_read_b128 v[18:21], v173 offset:4160
	v_add_f32_e32 v39, v39, v23
	v_add_f32_e32 v40, v40, v24
	v_add_f32_e32 v41, v41, v25
	ds_read_b128 v[22:25], v173 offset:4448
	v_mov_b32_e32 v34, s18
	v_mad_u32_u24 v34, v1, s23, v34
	v_add_u32_e32 v166, v34, v69
	v_cvt_pkrtz_f16_f32 v34, v2, v3
	v_cvt_pkrtz_f16_f32 v35, v71, v80
	v_cvt_pkrtz_f16_f32 v36, v81, v96
	v_cvt_pkrtz_f16_f32 v37, v97, v122
	ds_write_b128 v166, v[34:37]
	v_cvt_pkrtz_f16_f32 v34, v123, v127
	v_cvt_pkrtz_f16_f32 v35, v132, v133
	v_cvt_pkrtz_f16_f32 v36, v134, v135
	v_cvt_pkrtz_f16_f32 v37, v136, v137
	s_waitcnt lgkmcnt(2)
	v_add_f32_e32 v42, v42, v18
	v_add_f32_e32 v43, v43, v19
	v_add_f32_e32 v44, v44, v20
	v_add_f32_e32 v45, v45, v21
	s_waitcnt lgkmcnt(1)
	v_add_f32_e32 v46, v46, v22
	v_add_f32_e32 v47, v47, v23
	v_add_f32_e32 v48, v48, v24
	v_add_f32_e32 v49, v49, v25
	ds_write_b128 v166, v[34:37] offset:32
	v_cvt_pkrtz_f16_f32 v34, v138, v139
	v_cvt_pkrtz_f16_f32 v35, v140, v141
	v_cvt_pkrtz_f16_f32 v36, v38, v39
	v_cvt_pkrtz_f16_f32 v37, v40, v41
	ds_write_b128 v166, v[34:37] offset:64
	v_cvt_pkrtz_f16_f32 v34, v42, v43
	v_cvt_pkrtz_f16_f32 v35, v44, v45
	v_cvt_pkrtz_f16_f32 v36, v46, v47
	v_cvt_pkrtz_f16_f32 v37, v48, v49
	ds_write_b128 v166, v[34:37] offset:96
	ds_read_b128 v[34:37], v125 offset:16384
	v_lshrrev_b32_e32 v2, 2, v174
	v_mul_u32_u24_e32 v2, 0x48, v2
	v_lshlrev_b32_e32 v168, 1, v2
	v_add3_u32 v2, s21, v168, v160
	v_mfma_f32_32x32x16_f16 v[18:33], v[72:75], v[110:113], 0
	ds_read_b32 v2, v2 offset:4736
	ds_read_b128 v[72:75], v125 offset:17408
	v_mad_u32_u24 v71, v174, s15, v167
	s_waitcnt lgkmcnt(2)
	v_mfma_f32_32x32x16_f16 v[34:49], v[110:113], v[34:37], 0
	v_mfma_f32_32x32x16_f16 v[18:33], v[76:79], v[106:109], v[18:33]
	ds_read_b128 v[76:79], v125 offset:19456
	s_waitcnt lgkmcnt(1)
	v_mfma_f32_32x32x16_f16 v[34:49], v[106:109], v[72:75], v[34:49]
	ds_read_b128 v[72:75], v125 offset:18432
	s_waitcnt lgkmcnt(0)
	v_mfma_f32_32x32x16_f16 v[34:49], v[102:105], v[72:75], v[34:49]
	v_mfma_f32_32x32x16_f16 v[34:49], v[98:101], v[76:79], v[34:49]
	v_mfma_f32_32x32x16_f16 v[18:33], v[84:87], v[102:105], v[18:33]
	s_nop 10
	v_add_f32_e32 v3, v2, v34
	v_add_f32_e32 v34, v2, v35
	v_add_f32_e32 v35, v2, v36
	v_add_f32_e32 v36, v2, v37
	v_add_f32_e32 v37, v2, v38
	v_add_f32_e32 v38, v2, v39
	v_add_f32_e32 v39, v2, v40
	v_add_f32_e32 v40, v2, v41
	v_add_f32_e32 v41, v2, v42
	v_add_f32_e32 v42, v2, v43
	v_add_f32_e32 v43, v2, v44
	v_add_f32_e32 v44, v2, v45
	v_add_f32_e32 v45, v2, v46
	v_add_f32_e32 v46, v2, v47
	v_add_f32_e32 v47, v2, v48
	v_add_f32_e32 v2, v2, v49
	v_cvt_pkrtz_f16_f32 v34, v3, v34
	v_cvt_pkrtz_f16_f32 v35, v35, v36
	v_cvt_pkrtz_f16_f32 v36, v37, v38
	v_cvt_pkrtz_f16_f32 v37, v39, v40
	ds_write_b128 v71, v[34:37]
	v_cvt_pkrtz_f16_f32 v34, v41, v42
	v_cvt_pkrtz_f16_f32 v35, v43, v44
	v_cvt_pkrtz_f16_f32 v36, v45, v46
	v_cvt_pkrtz_f16_f32 v37, v47, v2
	ds_write_b128 v71, v[34:37] offset:32
	ds_read_b128 v[34:37], v125 offset:20480
	v_or_b32_e32 v2, 32, v174
	v_lshrrev_b32_e32 v2, 2, v2
	v_mul_u32_u24_e32 v2, 0x48, v2
	v_lshlrev_b32_e32 v169, 1, v2
	v_add3_u32 v2, s21, v169, v160
	v_mfma_f32_32x32x16_f16 v[18:33], v[88:91], v[98:101], v[18:33]
	ds_read_b32 v2, v2 offset:4736
	ds_read_b128 v[72:75], v125 offset:21504
	s_waitcnt lgkmcnt(2)
	v_mfma_f32_32x32x16_f16 v[34:49], v[110:113], v[34:37], 0
	s_nop 7
	v_fmamk_f32 v26, v54, 0x3eb8aa3b, v26
	v_fmamk_f32 v27, v55, 0x3eb8aa3b, v27
	v_fmamk_f32 v28, v56, 0x3eb8aa3b, v28
	v_fmamk_f32 v29, v57, 0x3eb8aa3b, v29
	ds_read_b128 v[54:57], v125 offset:22528
	v_fmamk_f32 v22, v58, 0x3eb8aa3b, v22
	v_fmamk_f32 v23, v59, 0x3eb8aa3b, v23
	s_waitcnt lgkmcnt(1)
	v_mfma_f32_32x32x16_f16 v[34:49], v[106:109], v[72:75], v[34:49]
	v_fmamk_f32 v24, v60, 0x3eb8aa3b, v24
	v_fmamk_f32 v25, v61, 0x3eb8aa3b, v25
	ds_read_b128 v[58:61], v125 offset:23552
	v_fmamk_f32 v18, v62, 0x3eb8aa3b, v18
	v_fmamk_f32 v19, v63, 0x3eb8aa3b, v19
	v_fmamk_f32 v20, v64, 0x3eb8aa3b, v20
	v_fmamk_f32 v21, v65, 0x3eb8aa3b, v21
	s_waitcnt lgkmcnt(1)
	v_mfma_f32_32x32x16_f16 v[34:49], v[102:105], v[54:57], v[34:49]
	v_fmamk_f32 v30, v50, 0x3eb8aa3b, v30
	v_fmamk_f32 v31, v51, 0x3eb8aa3b, v31
	v_fmamk_f32 v32, v52, 0x3eb8aa3b, v32
	v_fmac_f32_e32 v33, 0x3eb8aa3b, v53
	s_waitcnt lgkmcnt(0)
	v_mfma_f32_32x32x16_f16 v[34:49], v[98:101], v[58:61], v[34:49]
	s_nop 11
	v_add_f32_e32 v3, v2, v34
	v_add_f32_e32 v34, v2, v35
	v_add_f32_e32 v35, v2, v36
	v_add_f32_e32 v36, v2, v37
	v_add_f32_e32 v37, v2, v38
	v_add_f32_e32 v38, v2, v39
	v_add_f32_e32 v39, v2, v40
	v_add_f32_e32 v40, v2, v41
	v_add_f32_e32 v41, v2, v42
	v_add_f32_e32 v42, v2, v43
	v_add_f32_e32 v43, v2, v44
	v_add_f32_e32 v44, v2, v45
	v_add_f32_e32 v45, v2, v46
	v_add_f32_e32 v46, v2, v47
	v_add_f32_e32 v47, v2, v48
	v_add_f32_e32 v2, v2, v49
	v_cvt_pkrtz_f16_f32 v34, v3, v34
	v_cvt_pkrtz_f16_f32 v35, v35, v36
	v_cvt_pkrtz_f16_f32 v36, v37, v38
	v_cvt_pkrtz_f16_f32 v37, v39, v40
	ds_write_b128 v71, v[34:37] offset:8704
	v_cvt_pkrtz_f16_f32 v34, v41, v42
	v_cvt_pkrtz_f16_f32 v35, v43, v44
	v_cvt_pkrtz_f16_f32 v36, v45, v46
	v_cvt_pkrtz_f16_f32 v37, v47, v2
	ds_write_b128 v71, v[34:37] offset:8736
	s_waitcnt vmcnt(0) lgkmcnt(0)
	s_barrier
	s_cbranch_vccz .LBB2_82
	s_lshl_b32 s2, s22, 10
	s_add_i32 s23, s2, 0
	s_lshl_b64 s[2:3], s[14:15], 4
	s_add_i32 s21, s22, -8
	s_and_b32 s3, s3, 15
	s_and_b32 s2, s2, 0xfffffc00
	s_add_u32 s2, s16, s2
	s_addc_u32 s3, s17, s3
	v_lshl_add_u64 v[2:3], v[120:121], 1, s[2:3]
	s_mov_b64 s[2:3], 0x30000
	v_lshl_add_u64 v[2:3], v[2:3], 0, s[2:3]
	s_mov_b64 s[2:3], 0x2000
